# baseline (speedup 1.0000x reference)
_Z11prep_kernelPKfS0_S0_S0_S0_S0_S0_PKiPc:
	v_and_b32_e32 v18, 0x3ff, v0
	s_load_dwordx8 s[36:43], s[0:1], 0x0
	s_load_dwordx8 s[12:19], s[0:1], 0x20
	s_load_dwordx2 s[28:29], s[0:1], 0x40
	v_lshl_or_b32 v14, s2, 8, v18
	v_mov_b32_e32 v32, 0
	v_mov_b32_e32 v33, 0
	v_mov_b32_e32 v34, 0
	v_mov_b32_e32 v35, 0
	v_lshlrev_b32_e32 v36, 4, v14
	s_mov_b32 s3, 0x1e848
	v_mov_b32_e32 v1, 0x1e847
	v_cmp_gt_i32_e64 s[8:9], s3, v14
	v_mov_b32_e32 v17, 0
	v_ashrrev_i32_e32 v27, 6, v14
	v_cndmask_b32_e64 v1, v1, v14, s[8:9]
	v_lshlrev_b32_e32 v2, 1, v1
	v_ashrrev_i32_e32 v3, 31, v2
	s_waitcnt lgkmcnt(0)
	v_lshl_add_u64 v[10:11], v[2:3], 4, s[18:19]
	global_load_dwordx4 v[2:5], v[10:11], off offset:16
	global_load_dwordx4 v[6:9], v[10:11], off
	v_lshl_add_u32 v10, v1, 3, -1
	v_cmp_lt_i32_e32 vcc, 0, v1
	v_and_b32_e32 v28, 63, v0
	s_movk_i32 s3, 0x4000
	v_cndmask_b32_e32 v16, 0, v10, vcc
	v_lshl_add_u64 v[10:11], v[16:17], 2, s[18:19]
	global_load_dword v1, v[10:11], off
	v_min_i32_e32 v10, 0x7f, v27
	v_lshl_or_b32 v10, v10, 7, v28
	v_ashrrev_i32_e32 v11, 31, v10
	v_lshl_add_u64 v[10:11], v[10:11], 2, s[36:37]
	global_load_dword v29, v[10:11], off
	global_load_dword v26, v[10:11], off offset:256
	v_mov_b32_e32 v10, 0x3fff
	v_cmp_gt_i32_e32 vcc, s3, v14
	s_movk_i32 s3, 0x3000
	v_cmp_gt_i32_e64 s[4:5], s3, v14
	v_cndmask_b32_e32 v10, v10, v14, vcc
	v_ashrrev_i32_e32 v11, 31, v10
	v_lshl_add_u64 v[10:11], v[10:11], 2, s[12:13]
	global_load_dword v25, v[10:11], off
	v_mov_b32_e32 v10, 0x2fff
	v_cndmask_b32_e64 v10, v10, v14, s[4:5]
	v_ashrrev_i32_e32 v11, 31, v10
	v_lshl_add_u64 v[10:11], v[10:11], 2, s[14:15]
	s_movk_i32 s3, 0x1800
	global_load_dword v24, v[10:11], off
	v_mov_b32_e32 v10, 0x17ff
	v_cmp_gt_i32_e64 s[6:7], s3, v14
	s_movk_i32 s3, 0x80
	v_cmp_gt_i32_e64 s[10:11], s3, v14
	v_cndmask_b32_e64 v10, v10, v14, s[6:7]
	v_ashrrev_i32_e32 v11, 31, v10
	v_lshl_add_u64 v[10:11], v[10:11], 2, s[16:17]
	global_load_dword v23, v[10:11], off
	v_mov_b32_e32 v10, 0x7f
	v_cndmask_b32_e64 v10, v10, v14, s[10:11]
	v_ashrrev_i32_e32 v11, 31, v10
	v_lshlrev_b64 v[10:11], 2, v[10:11]
	v_lshl_add_u64 v[12:13], s[38:39], 0, v[10:11]
	global_load_dword v16, v[12:13], off
	v_lshl_add_u64 v[12:13], s[40:41], 0, v[10:11]
	v_lshl_add_u64 v[10:11], s[42:43], 0, v[10:11]
	global_load_dword v19, v[12:13], off
	global_load_dword v22, v[10:11], off
	v_lshlrev_b32_e32 v31, 2, v28
	global_load_dword v30, v31, s[38:39]
	global_load_dword v31, v31, s[38:39] offset:256
	s_add_u32 s44, s28, 0x200000
	s_addc_u32 s45, s29, 0
	s_add_u32 s46, s28, 0x400000
	s_addc_u32 s47, s29, 0
	s_add_u32 s48, s28, 0x600000
	s_addc_u32 s49, s29, 0
	global_store_dwordx4 v36, v[32:35], s[28:29] sc1
	global_store_dwordx4 v36, v[32:35], s[44:45] sc1
	global_store_dwordx4 v36, v[32:35], s[46:47] sc1
	global_store_dwordx4 v36, v[32:35], s[48:49] sc1
	s_cmp_gt_u32 s2, 15
	s_cbranch_scc1 .Lprep_nz5
	s_add_u32 s50, s28, 0x800000
	s_addc_u32 s51, s29, 0
	global_store_dwordx4 v36, v[32:35], s[50:51] sc1
.Lprep_nz5:
	v_ashrrev_i32_e32 v15, 31, v14
	v_mov_b32_e32 v10, 0
	s_and_saveexec_b64 s[12:13], s[8:9]
	s_cbranch_execz .LBB0_7
	s_waitcnt vmcnt(16)
	v_pk_mov_b32 v[20:21], v[2:3], v[4:5] op_sel:[1,0]
	s_waitcnt vmcnt(15)
	v_pk_mov_b32 v[12:13], v[8:9], v[2:3] op_sel:[1,0]
	v_cmp_lt_i32_e64 s[0:1], v4, v20
	v_pk_mov_b32 v[10:11], v[6:7], v[8:9] op_sel:[1,0]
	s_movk_i32 s3, 0xff
	v_cndmask_b32_e64 v20, 0, 1, s[0:1]
	v_cmp_lt_i32_e64 s[0:1], v5, v21
	v_lshlrev_b16_e32 v20, 2, v20
	s_nop 0
	v_cndmask_b32_e64 v21, 0, 1, s[0:1]
	v_cmp_lt_i32_e64 s[0:1], v3, v13
	v_lshlrev_b16_e32 v21, 3, v21
	v_or_b32_e32 v20, v21, v20
	v_cndmask_b32_e64 v13, 0, 1, s[0:1]
	v_cmp_lt_i32_e64 s[0:1], v2, v12
	v_lshlrev_b16_e32 v13, 1, v13
	s_nop 0
	v_cndmask_b32_e64 v12, 0, 1, s[0:1]
	v_cmp_lt_i32_e64 s[0:1], v8, v10
	v_or_b32_e32 v12, v12, v13
	v_bitop3_b16 v12, v12, v20, 3 bitop3:0xec
	v_cndmask_b32_e64 v10, 0, 1, s[0:1]
	v_cmp_lt_i32_e64 s[0:1], v9, v11
	v_lshlrev_b16_e32 v10, 2, v10
	v_lshlrev_b16_e32 v12, 4, v12
	v_cndmask_b32_e64 v11, 0, 1, s[0:1]
	v_lshlrev_b16_e32 v11, 3, v11
	v_cmp_lt_i32_e64 s[0:1], v7, v6
	v_or_b32_e32 v10, v11, v10
	s_nop 0
	v_cndmask_b32_e64 v11, 0, 1, s[0:1]
	s_waitcnt vmcnt(14)
	v_cmp_lt_i32_e64 s[0:1], v6, v1
	v_lshlrev_b16_e32 v11, 1, v11
	v_or_b32_e32 v6, v7, v6
	v_cndmask_b32_e64 v1, 0, 1, s[0:1]
	v_bitop3_b16 v1, v1, 3, v11 bitop3:0xc8
	v_or3_b32 v6, v6, v8, v9
	v_bitop3_b16 v1, v1, 15, v10 bitop3:0xc8
	v_or3_b32 v2, v6, v2, v3
	v_or3_b32 v2, v2, v4, v5
	s_movk_i32 s0, 0x3fff
	v_bitop3_b16 v1, v1, s3, v12 bitop3:0xc8
	v_cmp_lt_u32_e64 s[0:1], s0, v2
	v_cmp_ne_u16_e64 s[8:9], 0, v1
	s_or_b64 s[0:1], s[8:9], s[0:1]
	v_cndmask_b32_e64 v10, 0, 1, s[0:1]
.LBB0_7:
	s_or_b64 exec, exec, s[12:13]
	s_waitcnt vmcnt(14)
	v_cmp_ne_u32_e64 s[8:9], 0, v10
	v_lshrrev_b32_e32 v0, 6, v18
	v_lshlrev_b32_e32 v0, 2, v0
	s_cmp_lg_u64 s[8:9], 0
	s_cselect_b32 s3, 1, 0
	v_mov_b32_e32 v1, s3
	ds_write_b32 v0, v1
	s_waitcnt lgkmcnt(0)
	s_barrier
	v_cmp_eq_u32_e64 s[0:1], 0, v18
	s_and_saveexec_b64 s[8:9], s[0:1]
	s_cbranch_execz .LBB0_16
	v_mov_b32_e32 v0, 0
	ds_read_b128 v[4:7], v0
	s_mov_b32 s3, 0
	s_lshl_b64 s[0:1], s[2:3], 2
	s_add_u32 s0, s28, s0
	s_addc_u32 s1, s29, s1
	v_mov_b32_e32 v0, 0x829000
	s_waitcnt lgkmcnt(0)
	v_or_b32_e32 v1, v4, v5
	v_or3_b32 v1, v1, v6, v7
	global_store_dword v0, v1, s[0:1] offset:2048

.LBB0_22:
	s_waitcnt vmcnt(12)
	v_add_f32_e32 v0, v29, v26
	s_nop 1
	v_add_f32_dpp v0, v0, v0 quad_perm:[1,0,3,2] row_mask:0xf bank_mask:0xf bound_ctrl:1
	s_nop 1
	v_add_f32_dpp v0, v0, v0 quad_perm:[2,3,0,1] row_mask:0xf bank_mask:0xf bound_ctrl:1
	s_nop 1
	v_add_f32_dpp v0, v0, v0 row_half_mirror row_mask:0xf bank_mask:0xf bound_ctrl:1
	s_nop 1
	v_add_f32_dpp v0, v0, v0 row_mirror row_mask:0xf bank_mask:0xf bound_ctrl:1
	s_nop 1
	v_readlane_b32 s44, v0, 0
	v_readlane_b32 s45, v0, 16
	v_readlane_b32 s46, v0, 32
	v_readlane_b32 s47, v0, 48
	s_mov_b32 s8, 0x7ffff8
	v_bfe_u32 v2, v14, 6, 3
	v_lshrrev_b32_e32 v3, 8, v14
	s_add_u32 s0, s28, 0x810000
	s_addc_u32 s1, s29, 0
	v_mov_b32_e32 v4, s44
	v_add_f32_e32 v4, s45, v4
	v_add_f32_e32 v4, s46, v4
	v_add_f32_e32 v4, s47, v4
	v_lshrrev_b32_e32 v0, 4, v28
	v_and_or_b32 v0, v3, s8, v0
	v_lshlrev_b32_e32 v3, 1, v27
	v_and_b32_e32 v1, 15, v18
	v_lshlrev_b32_e32 v0, 6, v0
	v_and_b32_e32 v3, 48, v3
	v_or3_b32 v0, v0, v1, v3
	v_lshl_or_b32 v0, v0, 3, v2
	v_ashrrev_i32_e32 v1, 31, v0
	v_fmac_f32_e32 v29, 0xbc000000, v4
	v_lshl_add_u64 v[2:3], v[0:1], 1, s[0:1]
	v_or_b32_e32 v0, 0x800, v0
	v_cvt_pk_bf16_f32 v5, v29, s0
	v_fmac_f32_e32 v26, 0xbc000000, v4
	v_ashrrev_i32_e32 v1, 31, v0
	global_store_short v[2:3], v5, off
	v_cvt_pk_bf16_f32 v2, v26, s0
	v_lshl_add_u64 v[0:1], v[0:1], 1, s[0:1]
	global_store_short v[0:1], v2, off
	s_or_b64 exec, exec, s[2:3]
	s_and_saveexec_b64 s[0:1], vcc
	s_cbranch_execz .LBB0_18
.LBB0_23:
	v_lshrrev_b32_e32 v0, 25, v15
	v_add_u32_e32 v0, v14, v0
	v_ashrrev_i32_e32 v1, 7, v0
	v_and_b32_e32 v0, 0xffffff80, v0
	v_sub_u32_e32 v0, v14, v0
	v_lshrrev_b32_e32 v5, 2, v1
	v_and_b32_e32 v3, 15, v0
	v_and_b32_e32 v5, 4, v5
	v_lshrrev_b32_e32 v0, 2, v0
	v_lshrrev_b32_e32 v4, 5, v1
	v_and_or_b32 v5, v1, 3, v5
	v_and_b32_e32 v0, 0x7ffffc, v0
	v_lshlrev_b32_e32 v1, 2, v1
	v_add_lshl_u32 v0, v0, v4, 6
	v_and_b32_e32 v1, 48, v1
	v_or3_b32 v0, v0, v3, v1
	v_lshl_or_b32 v0, v0, 3, v5
	v_ashrrev_i32_e32 v1, 31, v0
	v_lshl_add_u64 v[0:1], v[0:1], 1, s[28:29]
	v_add_co_u32_e32 v0, vcc, 0x818000, v0
	s_waitcnt vmcnt(11)
	v_cvt_pk_bf16_f32 v2, v25, s0
	v_addc_co_u32_e32 v1, vcc, 0, v1, vcc
	global_store_short v[0:1], v2, off offset:2048
	s_or_b64 exec, exec, s[0:1]
	s_and_saveexec_b64 s[0:1], s[4:5]
	s_cbranch_execz .LBB0_19
.LBB0_24:
	s_mov_b32 s2, 0x2aaaaaab
	v_mul_hi_i32 v0, v14, s2
	v_lshrrev_b32_e32 v1, 31, v0
	v_ashrrev_i32_e32 v0, 4, v0
	v_add_u32_e32 v0, v0, v1
	s_movk_i32 s2, 0x60
	v_mul_lo_u32 v1, v0, s2
	v_sub_u32_e32 v1, v14, v1
	v_lshrrev_b32_e32 v5, 2, v0
	v_and_b32_e32 v3, 15, v1
	v_and_b32_e32 v5, 4, v5
	v_lshrrev_b32_e32 v1, 2, v1
	v_lshrrev_b32_e32 v4, 5, v0
	v_and_or_b32 v5, v0, 3, v5
	v_and_b32_e32 v1, 0x7ffffc, v1
	v_lshlrev_b32_e32 v0, 2, v0
	v_add_lshl_u32 v1, v1, v4, 6
	v_and_b32_e32 v0, 48, v0
	v_or3_b32 v0, v1, v3, v0
	v_lshl_or_b32 v0, v0, 3, v5
	v_ashrrev_i32_e32 v1, 31, v0
	v_lshl_add_u64 v[0:1], v[0:1], 1, s[28:29]
	v_add_co_u32_e32 v0, vcc, 0x820000, v0
	s_waitcnt vmcnt(10)
	v_cvt_pk_bf16_f32 v2, v24, s0
	v_addc_co_u32_e32 v1, vcc, 0, v1, vcc
	global_store_short v[0:1], v2, off offset:2048
	s_or_b64 exec, exec, s[0:1]
	s_and_saveexec_b64 s[0:1], s[6:7]
	s_cbranch_execz .LBB0_20
.LBB0_25:
	v_lshrrev_b32_e32 v0, 26, v15
	v_add_u32_e32 v0, v14, v0
	v_ashrrev_i32_e32 v1, 6, v0
	v_and_b32_e32 v0, 0xffffffc0, v0
	v_sub_u32_e32 v0, v14, v0
	v_lshrrev_b32_e32 v5, 2, v1
	v_lshrrev_b32_e32 v3, 4, v0
	v_and_b32_e32 v5, 4, v5
	v_lshrrev_b32_e32 v4, 5, v1
	v_and_or_b32 v5, v1, 3, v5
	v_lshl_add_u32 v3, v3, 1, v3
	v_lshlrev_b32_e32 v1, 2, v1
	v_and_b32_e32 v0, 15, v0
	v_add_lshl_u32 v3, v3, v4, 6
	v_and_b32_e32 v1, 48, v1
	v_or3_b32 v0, v3, v0, v1
	v_lshl_or_b32 v0, v0, 3, v5
	v_ashrrev_i32_e32 v1, 31, v0
	v_lshl_add_u64 v[0:1], v[0:1], 1, s[28:29]
	v_add_co_u32_e32 v0, vcc, 0x826000, v0
	s_waitcnt vmcnt(9)
	v_cvt_pk_bf16_f32 v2, v23, s0
	v_addc_co_u32_e32 v1, vcc, 0, v1, vcc
	global_store_short v[0:1], v2, off offset:2048
	s_or_b64 exec, exec, s[0:1]
	s_and_saveexec_b64 s[0:1], s[10:11]
	s_cbranch_execz .LBB0_21
